# attention-A: expert-weight staging DMA issued from a running pointer/slot/rotated offset (7 instr instead of 19-21 per tile), group finish block moved out of line
# speedup vs baseline: 1.0754x; 1.0015x over previous
.Lpro_noconv:
	s_cmp_lg_u64 s[12:13], 0
	s_cselect_b64 s[54:55], -1, 0
	s_cmp_lt_u32 s0, 2
	s_mov_b32 s0, 0x3f400000
	s_cselect_b64 s[52:53], -1, 0
	s_mov_b32 s8, s9
	v_mfma_scale_f32_32x32x64_f8f6f4 v[16:31], v[12:17], v[182:187], 0, v217, v216 op_sel_hi:[0,0,0] cbsz:2 blgp:2
	s_nop 4
	v_max_f32_e32 v52, v33, v33
	v_max_f32_e32 v53, v32, v32
	v_max_f32_e32 v52, v53, v52
	v_max3_f32 v52, v52, v34, v35
	v_max3_f32 v52, v52, v36, v37
	v_max3_f32 v52, v52, v38, v39
	v_max3_f32 v52, v52, v40, v41
	v_mfma_scale_f32_32x32x64_f8f6f4 v[16:31], v[58:63], v[176:181], v[16:31], v217, v216 op_sel_hi:[0,0,0] cbsz:2 blgp:2
	v_max3_f32 v52, v52, v42, v43
	v_max3_f32 v52, v52, v44, v45
	v_max3_f32 v52, v52, v46, v47
	s_mov_b32 s10, s9
	s_mov_b32 s11, s9
	s_mov_b32 s12, s9
	s_mov_b32 s13, s9
	s_nop 4
	v_max3_f32 v52, v52, v16, v17
	v_max3_f32 v52, v52, v18, v19
	v_max3_f32 v52, v52, v20, v21
	v_max3_f32 v52, v52, v22, v23
	v_max3_f32 v52, v52, v24, v25
	v_max3_f32 v52, v52, v26, v27
	v_max3_f32 v52, v52, v28, v29
	v_max3_f32 v52, v52, v30, v31
	v_mov_b32_e32 v53, v52
	s_nop 1
	v_permlane32_swap_b32_e32 v52, v53
	v_max_f32_e32 v53, v53, v53
	v_max_f32_e32 v52, v52, v52
	v_max_f32_e32 v52, v52, v53
	v_add_f32_e32 v53, 0x7149f2ca, v52
	v_cmp_ge_f32_e32 vcc, s0, v53
	v_max_f32_e32 v52, 0xf149f2ca, v52
	s_cmp_lg_u64 vcc, exec
	v_add_f32_e32 v52, 2.0, v52
	s_cselect_b64 vcc, -1, 0
	v_cndmask_b32_e32 v52, v219, v52, vcc
	v_add_f32_e32 v53, -4.0, v52
	s_lshl_b32 s0, s46, 2
	v_sub_f32_e32 v32, v32, v53
	v_sub_f32_e32 v33, v33, v53
	v_sub_f32_e32 v34, v34, v53
	v_sub_f32_e32 v35, v35, v53
	v_sub_f32_e32 v36, v36, v53
	v_sub_f32_e32 v37, v37, v53
	v_sub_f32_e32 v38, v38, v53
	v_sub_f32_e32 v39, v39, v53
	v_sub_f32_e32 v40, v40, v53
	v_sub_f32_e32 v41, v41, v53
	v_sub_f32_e32 v42, v42, v53
	v_sub_f32_e32 v43, v43, v53
	v_sub_f32_e32 v44, v44, v53
	v_sub_f32_e32 v45, v45, v53
	v_sub_f32_e32 v46, v46, v53
	v_sub_f32_e32 v47, v47, v53
	s_add_i32 s0, s0, 0
	s_mov_b32 s14, s9
	s_mov_b32 s15, s9
	s_mov_b32 s16, s9
	s_mov_b32 s17, s9
	s_mov_b32 s18, s9
	s_mov_b32 s19, s9
	s_mov_b32 s20, s9
	s_mov_b32 s21, s9
	s_mov_b32 s22, s9
	s_mov_b32 s23, s9
	v_mov_b64_e32 v[0:1], s[8:9]
	v_exp_f32_e32 v144, v32
	v_exp_f32_e32 v145, v33
	v_exp_f32_e32 v146, v34
	v_exp_f32_e32 v147, v35
	v_exp_f32_e32 v148, v36
	v_exp_f32_e32 v149, v37
	v_exp_f32_e32 v150, v38
	v_exp_f32_e32 v151, v39
	v_exp_f32_e32 v152, v40
	v_exp_f32_e32 v153, v41
	v_exp_f32_e32 v154, v42
	v_exp_f32_e32 v155, v43
	v_exp_f32_e32 v156, v44
	v_exp_f32_e32 v157, v45
	v_exp_f32_e32 v158, v46
	v_exp_f32_e32 v159, v47
	s_add_i32 s0, s0, 0x1c800
	v_mov_b64_e32 v[2:3], s[10:11]
	v_mov_b64_e32 v[4:5], s[12:13]
	v_mov_b64_e32 v[6:7], s[14:15]
	v_mov_b64_e32 v[8:9], s[16:17]
	v_mov_b64_e32 v[10:11], s[18:19]
	v_mov_b64_e32 v[12:13], s[20:21]
	v_mov_b64_e32 v[14:15], s[22:23]
	v_sub_f32_e32 v128, v16, v53
	s_and_b64 s[10:11], s[52:53], exec
	v_lshlrev_b32_e32 v16, 7, v48
	v_sub_f32_e32 v80, 4.0, v52
	v_sub_f32_e32 v143, v31, v53
	v_sub_f32_e32 v142, v30, v53
	v_sub_f32_e32 v141, v29, v53
	v_sub_f32_e32 v140, v28, v53
	v_sub_f32_e32 v139, v27, v53
	v_sub_f32_e32 v138, v26, v53
	v_sub_f32_e32 v137, v25, v53
	v_sub_f32_e32 v136, v24, v53
	v_sub_f32_e32 v135, v23, v53
	v_sub_f32_e32 v134, v22, v53
	v_sub_f32_e32 v133, v21, v53
	v_sub_f32_e32 v132, v20, v53
	v_sub_f32_e32 v131, v19, v53
	v_sub_f32_e32 v130, v18, v53
	v_sub_f32_e32 v129, v17, v53
	s_cselect_b32 s14, 23, 22
	v_add3_u32 v164, s85, v16, v51
	s_add_u32 s10, s78, s4
	v_add_u32_e32 v174, v49, v50
	v_mov_b64_e32 v[62:63], v[14:15]
	v_mov_b64_e32 v[46:47], v[14:15]
	v_mov_b64_e32 v[30:31], v[14:15]
	v_mov_b64_e32 v[78:79], v[14:15]
	s_mov_b32 s1, 2
	s_mov_b32 s57, 1
	s_mov_b32 s27, -2
	v_mov_b32_e32 v81, v80
	v_mov_b32_e32 v82, v80
	v_mov_b32_e32 v83, v80
	v_mov_b32_e32 v84, v80
	v_mov_b32_e32 v85, v80
	v_mov_b32_e32 v86, v80
	v_mov_b32_e32 v87, v80
	v_mov_b32_e32 v88, v80
	v_mov_b32_e32 v89, v80
	v_mov_b32_e32 v90, v80
	v_mov_b32_e32 v91, v80
	v_mov_b32_e32 v92, v80
	v_mov_b32_e32 v93, v80
	v_mov_b32_e32 v94, v80
	v_mov_b32_e32 v95, v80
	s_mov_b32 s15, 0
	v_mov_b32_e32 v165, v167
	s_addc_u32 s11, s79, s5
	v_mov_b32_e32 v175, v167
	v_mov_b64_e32 v[60:61], v[12:13]
	v_mov_b64_e32 v[58:59], v[10:11]
	v_mov_b64_e32 v[56:57], v[8:9]
	v_mov_b64_e32 v[54:55], v[6:7]
	v_mov_b64_e32 v[52:53], v[4:5]
	v_mov_b64_e32 v[50:51], v[2:3]
	v_mov_b64_e32 v[48:49], v[0:1]
	v_mov_b64_e32 v[44:45], v[12:13]
	v_mov_b64_e32 v[42:43], v[10:11]
	v_mov_b64_e32 v[40:41], v[8:9]
	v_mov_b64_e32 v[38:39], v[6:7]
	v_mov_b64_e32 v[36:37], v[4:5]
	v_mov_b64_e32 v[34:35], v[2:3]
	v_mov_b64_e32 v[32:33], v[0:1]
	v_mov_b64_e32 v[28:29], v[12:13]
	v_mov_b64_e32 v[26:27], v[10:11]
	v_mov_b64_e32 v[24:25], v[8:9]
	v_mov_b64_e32 v[22:23], v[6:7]
	v_mov_b64_e32 v[20:21], v[4:5]
	v_mov_b64_e32 v[18:19], v[2:3]
	v_mov_b64_e32 v[16:17], v[0:1]
	s_mov_b32 s16, 2
	v_mov_b64_e32 v[76:77], v[12:13]
	v_mov_b64_e32 v[74:75], v[10:11]
	v_mov_b64_e32 v[72:73], v[8:9]
	v_mov_b64_e32 v[70:71], v[6:7]
	v_mov_b64_e32 v[68:69], v[4:5]
	v_mov_b64_e32 v[66:67], v[2:3]
	v_mov_b64_e32 v[64:65], v[0:1]
	v_mbcnt_lo_u32_b32 v200, -1, 0
	v_mbcnt_hi_u32_b32 v200, -1, v200
	v_lshrrev_b32_e32 v201, 3, v200
	v_mul_lo_u32 v201, v201, s56
	v_lshlrev_b32_e32 v200, 4, v200
	v_and_b32_e32 v200, 0x70, v200
	v_lshl_or_b32 v214, v201, 2, v200
	v_mov_b32_e32 v215, v214
	s_mov_b64 s[98:99], s[58:59]
	s_add_i32 s100, s66, 0xc800
	s_lshl_b32 s101, s56, 5
	s_movk_i32 s17, 0x70
	ds_read_b128 v[228:231], v223 offset:8192
	ds_read_b64 v[232:233], v224 offset:8192
	ds_read_b128 v[234:237], v223 offset:12288
	ds_read_b64 v[238:239], v224 offset:12288
	ds_read_b128 v[240:243], v221 offset:8192
	ds_read_b64 v[244:245], v222 offset:8192
	ds_read_b128 v[246:249], v221 offset:12288
	ds_read_b64 v[250:251], v222 offset:12288

.LBB0_417:
	s_add_u32 s12, s10, 0x74006000
	s_addc_u32 s13, s11, 0
	s_barrier
	s_add_i32 m0, s89, 0x2000
	s_add_u32 s4, s10, 0x74802000
	global_load_lds_dwordx4 v164, s[12:13]
	s_addc_u32 s5, s11, 0
	s_add_i32 m0, s89, 0x8000
	s_andn2_b64 vcc, exec, s[62:63]
	global_load_lds_dwordx4 v174, s[4:5]
	s_cbranch_vccnz .LBB0_419
	s_add_u32 s98, s98, s101
	s_addc_u32 s99, s99, 0
	s_add_i32 s100, s100, 0x400
	s_mov_b32 m0, s100
	v_add_u32_e32 v96, -16, v215
	v_bfi_b32 v215, s17, v96, v215
	global_load_lds_dwordx4 v215, s[98:99] nt

.LBB0_428:
	s_add_u32 s12, s10, 0x74008000
	s_addc_u32 s13, s11, 0
	s_barrier
	s_mov_b32 m0, s89
	s_add_u32 s4, s10, 0x74804000
	global_load_lds_dwordx4 v164, s[12:13]
	s_addc_u32 s5, s11, 0
	s_add_i32 m0, s89, 0x6000
	s_and_b64 vcc, exec, s[60:61]
	global_load_lds_dwordx4 v174, s[4:5]
	s_cbranch_vccnz .LBB0_437
	s_bfe_u32 s4, s1, 0x30000
	s_cbranch_scc0 .LBB0_432
	s_add_u32 s98, s98, s101
	s_addc_u32 s99, s99, 0
	s_add_i32 s100, s100, 0x400
	s_mov_b32 m0, s100
	v_add_u32_e32 v128, -16, v215
	v_bfi_b32 v215, s17, v128, v215
	global_load_lds_dwordx4 v215, s[98:99] nt

.LBB0_445:
	v_mov_b32_e32 v213, v212
	s_nop 1
	v_permlane32_swap_b32_e32 v212, v213
	v_max_f32_e32 v213, v213, v213
	v_max_f32_e32 v212, v212, v212
	v_max_f32_e32 v212, v212, v213
	v_add_f32_e32 v166, -4.0, v212
	v_add_f32_e32 v166, 1.0, v166
	v_max_f32_e32 v212, 0, v166
	v_exp_f32_e64 v166, -v212
	v_pk_add_f32 v[144:145], v[144:145], v[212:213] op_sel_hi:[1,0] neg_lo:[0,1] neg_hi:[0,1]
	v_pk_add_f32 v[146:147], v[146:147], v[212:213] op_sel_hi:[1,0] neg_lo:[0,1] neg_hi:[0,1]
	v_pk_add_f32 v[148:149], v[148:149], v[212:213] op_sel_hi:[1,0] neg_lo:[0,1] neg_hi:[0,1]
	v_pk_add_f32 v[150:151], v[150:151], v[212:213] op_sel_hi:[1,0] neg_lo:[0,1] neg_hi:[0,1]
	v_pk_add_f32 v[152:153], v[152:153], v[212:213] op_sel_hi:[1,0] neg_lo:[0,1] neg_hi:[0,1]
	v_pk_add_f32 v[154:155], v[154:155], v[212:213] op_sel_hi:[1,0] neg_lo:[0,1] neg_hi:[0,1]
	v_pk_add_f32 v[156:157], v[156:157], v[212:213] op_sel_hi:[1,0] neg_lo:[0,1] neg_hi:[0,1]
	v_pk_add_f32 v[158:159], v[158:159], v[212:213] op_sel_hi:[1,0] neg_lo:[0,1] neg_hi:[0,1]
	v_sub_f32_e32 v143, v143, v212
	v_sub_f32_e32 v142, v142, v212
	v_sub_f32_e32 v141, v141, v212
	v_sub_f32_e32 v140, v140, v212
	v_sub_f32_e32 v139, v139, v212
	v_sub_f32_e32 v138, v138, v212
	v_sub_f32_e32 v137, v137, v212
	v_sub_f32_e32 v136, v136, v212
	v_sub_f32_e32 v135, v135, v212
	v_sub_f32_e32 v134, v134, v212
	v_sub_f32_e32 v133, v133, v212
	v_sub_f32_e32 v132, v132, v212
	v_sub_f32_e32 v131, v131, v212
	v_sub_f32_e32 v130, v130, v212
	v_sub_f32_e32 v129, v129, v212
	v_sub_f32_e32 v128, v128, v212
	v_sub_f32_e32 v95, v95, v212
	v_sub_f32_e32 v94, v94, v212
	v_sub_f32_e32 v93, v93, v212
	v_sub_f32_e32 v92, v92, v212
	v_sub_f32_e32 v91, v91, v212
	v_sub_f32_e32 v90, v90, v212
	v_sub_f32_e32 v89, v89, v212
	v_sub_f32_e32 v88, v88, v212
	v_sub_f32_e32 v87, v87, v212
	v_sub_f32_e32 v86, v86, v212
	v_sub_f32_e32 v85, v85, v212
	v_sub_f32_e32 v84, v84, v212
	v_sub_f32_e32 v83, v83, v212
	v_sub_f32_e32 v82, v82, v212
	v_sub_f32_e32 v81, v81, v212
	v_sub_f32_e32 v80, v80, v212
	s_branch .LBB0_438
.LBB0_432:
	s_waitcnt vmcnt(2)
	v_mbcnt_lo_u32_b32 v138, -1, 0
	v_mbcnt_hi_u32_b32 v138, -1, v138
	s_lshr_b32 s8, s1, 3
	s_add_i32 s12, s8, -1
	s_ashr_i32 s13, s12, 31
	s_lshl_b64 s[12:13], s[12:13], s14
	s_add_u32 s12, s50, s12
	s_addc_u32 s13, s51, s13
	s_lshl_b64 s[18:19], s[48:49], 3
	v_and_b32_e32 v137, 7, v138
	v_ashrrev_i32_e32 v136, 3, v138
	v_lshlrev_b32_e32 v146, 2, v138
	s_andn2_b64 vcc, exec, s[54:55]
	v_lshl_add_u32 v147, v137, 10, s66
	v_lshlrev_b32_e32 v148, 2, v136
	v_and_b32_e32 v148, 12, v148
	v_add_u32_e32 v147, 0xc800, v147
	v_add_u32_e32 v147, v147, v148
	v_add_u32_e32 v150, v136, v146
	v_add_u32_e32 v151, 8, v150
	v_add_u32_e32 v152, 16, v150
	v_add_u32_e32 v153, 24, v150
	v_and_b32_e32 v150, 28, v150
	v_and_b32_e32 v151, 28, v151
	v_and_b32_e32 v152, 28, v152
	v_and_b32_e32 v153, 28, v153
	v_lshl_add_u32 v150, v150, 2, v147
	v_lshl_add_u32 v151, v151, 2, v147
	v_lshl_add_u32 v152, v152, 2, v147
	v_lshl_add_u32 v153, v153, 2, v147
	s_cbranch_vccnz .Lfin_nog
	v_lshl_add_u32 v132, v137, 5, s0
	ds_read_b128 v[128:131], v132
	ds_read_b128 v[140:143], v132 offset:16

.Lfin_go:
	v_lshl_add_u64 v[142:143], s[44:45], 0, v[136:137]
	v_mov_b64_e32 v[138:139], s[12:13]
	v_mad_u64_u32 v[144:145], s[12:13], v142, s48, v[138:139]
	v_mul_lo_u32 v139, v142, s49
	v_mul_lo_u32 v142, v143, s48
	v_add3_u32 v145, v142, v145, v139
	v_lshl_add_u64 v[142:143], v[144:145], 0, s[46:47]
	v_lshl_add_u64 v[142:143], v[142:143], 0, v[166:167]
	v_pk_mul_f32 v[188:189], v[188:189], v[134:135]
	v_pk_mul_f32 v[190:191], v[190:191], v[132:133]
	v_pk_mul_f32 v[192:193], v[192:193], v[130:131]
	v_pk_mul_f32 v[194:195], v[194:195], v[128:129]
	v_cvt_pk_fp8_f32 v140, v188, v189
	v_cvt_pk_fp8_f32 v141, v192, v193
	v_cvt_pk_fp8_f32 v140, v190, v191 op_sel:[0,0,1]
	v_cvt_pk_fp8_f32 v141, v194, v195 op_sel:[0,0,1]
	s_nop 1
	global_store_dwordx2 v[142:143], v[140:141], off nt
	v_lshl_add_u64 v[142:143], v[142:143], 0, s[18:19]
	s_nop 0
	v_pk_mul_f32 v[196:197], v[196:197], v[134:135]
	v_pk_mul_f32 v[198:199], v[198:199], v[132:133]
	v_pk_mul_f32 v[200:201], v[200:201], v[130:131]
	v_pk_mul_f32 v[202:203], v[202:203], v[128:129]
	v_cvt_pk_fp8_f32 v140, v196, v197
	v_cvt_pk_fp8_f32 v141, v200, v201
	v_cvt_pk_fp8_f32 v140, v198, v199 op_sel:[0,0,1]
	v_cvt_pk_fp8_f32 v141, v202, v203 op_sel:[0,0,1]
	s_nop 1
	global_store_dwordx2 v[142:143], v[140:141], off nt
	v_lshl_add_u64 v[142:143], v[142:143], 0, s[18:19]
	s_nop 0
	v_pk_mul_f32 v[204:205], v[204:205], v[134:135]
	v_pk_mul_f32 v[206:207], v[206:207], v[132:133]
	v_pk_mul_f32 v[208:209], v[208:209], v[130:131]
	v_pk_mul_f32 v[210:211], v[210:211], v[128:129]
	v_cvt_pk_fp8_f32 v140, v204, v205
	v_cvt_pk_fp8_f32 v141, v208, v209
	v_cvt_pk_fp8_f32 v140, v206, v207 op_sel:[0,0,1]
	v_cvt_pk_fp8_f32 v141, v210, v211 op_sel:[0,0,1]
	s_nop 1
	global_store_dwordx2 v[142:143], v[140:141], off nt
	v_lshl_add_u64 v[142:143], v[142:143], 0, s[18:19]
	s_nop 0
	v_pk_mul_f32 v[154:155], v[154:155], v[134:135]
	v_pk_mul_f32 v[156:157], v[156:157], v[132:133]
	v_pk_mul_f32 v[158:159], v[158:159], v[130:131]
	v_pk_mul_f32 v[212:213], v[212:213], v[128:129]
	v_cvt_pk_fp8_f32 v140, v154, v155
	v_cvt_pk_fp8_f32 v141, v158, v159
	v_cvt_pk_fp8_f32 v140, v156, v157 op_sel:[0,0,1]
	v_cvt_pk_fp8_f32 v141, v212, v213 op_sel:[0,0,1]
	s_nop 1
	global_store_dwordx2 v[142:143], v[140:141], off nt
	s_lshl_b64 s[98:99], s[8:9], 24
	s_add_u32 s98, s58, s98
	s_addc_u32 s99, s59, s99
	s_add_i32 s100, s66, 0xc800
	v_mov_b32_e32 v215, v214
	s_mov_b32 m0, s100
	s_nop 0
	global_load_lds_dwordx4 v215, s[98:99] nt
	s_branch .LBB0_437
